# v50 with spacer lengths A=1 B=2 (x64 cycles) after the sub-head-0 softmax
# baseline (speedup 1.0000x reference)
.LBB0_215:
	v_add_u32_e32 v212, s56, v225
	v_add_u32_e32 v6, v212, v227
	v_add_u32_e32 v7, v212, v228
	ds_read_b128 v[244:247], v6
	ds_read_b128 v[248:251], v6 offset:8192
	ds_read_b128 v[236:239], v7
	ds_read_b128 v[240:243], v7 offset:8192
	v_add_u32_e32 v6, v212, v229
	v_add_u32_e32 v7, v212, v230
	ds_read_b128 v[2:5], v6
	ds_read_b128 v[8:11], v6 offset:8192
	ds_read_b128 v[208:211], v7
	s_xor_b64 s[44:45], s[44:45], -1
	v_add_u32_e32 v6, v212, v226
	s_waitcnt lgkmcnt(6)
	v_mfma_f32_32x32x16_bf16 v[160:175], v[244:247], v[176:179], v[160:175]
	ds_read_b128 v[244:247], v7 offset:8192
	s_waitcnt lgkmcnt(6)
	v_mfma_f32_32x32x16_bf16 v[144:159], v[248:251], v[176:179], v[144:159]
	s_waitcnt lgkmcnt(5)
	v_mfma_f32_32x32x16_bf16 v[160:175], v[236:239], v[180:183], v[160:175]
	v_add_u32_e32 v7, v212, v231
	s_waitcnt lgkmcnt(4)
	v_mfma_f32_32x32x16_bf16 v[144:159], v[240:243], v[180:183], v[144:159]
	ds_read_b128 v[248:251], v6
	ds_read_b128 v[236:239], v6 offset:8192
	ds_read_b128 v[240:243], v7
	s_waitcnt lgkmcnt(6)
	v_mfma_f32_32x32x16_bf16 v[160:175], v[2:5], v[184:187], v[160:175]
	s_waitcnt lgkmcnt(5)
	v_mfma_f32_32x32x16_bf16 v[144:159], v[8:11], v[184:187], v[144:159]
	s_waitcnt lgkmcnt(4)
	v_mfma_f32_32x32x16_bf16 v[160:175], v[208:211], v[188:191], v[160:175]
	s_waitcnt lgkmcnt(3)
	v_mfma_f32_32x32x16_bf16 v[144:159], v[244:247], v[188:191], v[144:159]
	ds_read_b128 v[244:247], v7 offset:8192
	s_nop 9
	v_exp_f32_e32 v6, v160
	v_exp_f32_e32 v3, v161
	v_exp_f32_e32 v10, v164
	v_exp_f32_e32 v11, v165
	v_exp_f32_e32 v160, v172
	v_exp_f32_e32 v161, v173
	v_exp_f32_e32 v5, v162
	v_exp_f32_e32 v2, v144
	v_exp_f32_e32 v7, v146
	v_exp_f32_e32 v144, v148
	v_exp_f32_e32 v146, v150
	v_exp_f32_e32 v148, v168
	v_exp_f32_e32 v150, v169
	v_exp_f32_e32 v4, v145
	v_exp_f32_e32 v145, v149
	v_exp_f32_e32 v12, v166
	v_exp_f32_e32 v149, v152
	v_exp_f32_e32 v152, v170
	v_exp_f32_e32 v162, v174
	v_exp_f32_e32 v8, v163
	v_exp_f32_e32 v9, v147
	v_exp_f32_e32 v13, v167
	v_exp_f32_e32 v147, v151
	v_exp_f32_e32 v151, v153
	v_exp_f32_e32 v153, v154
	v_exp_f32_e32 v154, v171
	v_exp_f32_e32 v163, v175
	v_exp_f32_e32 v156, v156
	v_exp_f32_e32 v157, v157
	v_add_f32_e32 v164, v6, v3
	v_add_f32_e32 v165, v10, v11
	v_add_f32_e32 v166, v148, v150
	v_add_f32_e32 v167, v160, v161
	v_exp_f32_e32 v158, v158
	v_add_f32_e32 v164, v5, v164
	v_add_f32_e32 v165, v12, v165
	v_add_f32_e32 v166, v152, v166
	v_add_f32_e32 v167, v162, v167
	v_exp_f32_e32 v155, v155
	v_exp_f32_e32 v159, v159
	v_add_f32_e32 v164, v8, v164
	v_add_f32_e32 v165, v13, v165
	v_add_f32_e32 v166, v154, v166
	v_add_f32_e32 v167, v163, v167
	v_add_f32_e32 v164, v2, v164
	v_add_f32_e32 v165, v144, v165
	v_add_f32_e32 v166, v149, v166
	v_add_f32_e32 v167, v156, v167
	v_add_f32_e32 v164, v4, v164
	v_add_f32_e32 v165, v145, v165
	v_add_f32_e32 v166, v151, v166
	v_add_f32_e32 v167, v157, v167
	v_add_f32_e32 v164, v7, v164
	v_add_f32_e32 v165, v146, v165
	v_add_f32_e32 v166, v153, v166
	v_add_f32_e32 v167, v158, v167
	v_add_f32_e32 v164, v9, v164
	v_add_f32_e32 v165, v147, v165
	v_add_f32_e32 v166, v155, v166
	v_add_f32_e32 v167, v159, v167
	v_add_f32_e32 v164, v164, v165
	v_add_f32_e32 v165, v166, v167
	v_add_f32_e32 v213, v164, v165
	v_mov_b32_e32 v218, v213
	v_cvt_pk_bf16_f32 v208, v6, v3
	v_cvt_pk_bf16_f32 v209, v5, v8
	v_cvt_pk_bf16_f32 v210, v10, v11
	v_cvt_pk_bf16_f32 v211, v12, v13
	v_cvt_pk_bf16_f32 v10, v148, v150
	v_cvt_pk_bf16_f32 v11, v152, v154
	v_cvt_pk_bf16_f32 v12, v160, v161
	v_cvt_pk_bf16_f32 v13, v162, v163
	v_cvt_pk_bf16_f32 v6, v2, v4
	v_cvt_pk_bf16_f32 v7, v7, v9
	v_cvt_pk_bf16_f32 v8, v144, v145
	v_cvt_pk_bf16_f32 v9, v146, v147
	v_cvt_pk_bf16_f32 v2, v149, v151
	v_cvt_pk_bf16_f32 v3, v153, v155
	v_cvt_pk_bf16_f32 v4, v156, v157
	v_cvt_pk_bf16_f32 v5, v158, v159
	v_permlane32_swap_b32_e32 v213, v218
	v_permlane32_swap_b32_e32 v208, v210
	v_permlane32_swap_b32_e32 v209, v211
	v_permlane32_swap_b32_e32 v10, v12
	v_permlane32_swap_b32_e32 v11, v13
	v_permlane32_swap_b32_e32 v6, v8
	v_permlane32_swap_b32_e32 v7, v9
	v_permlane32_swap_b32_e32 v2, v4
	v_permlane32_swap_b32_e32 v3, v5
	s_nop 15
	v_mov_b32_e32 v160, 0
	s_andn2_b64 vcc, exec, s[44:45]
	v_mov_b32_e32 v161, 0
	v_mov_b32_e32 v162, 0
	v_mov_b32_e32 v163, 0
	v_mov_b32_e32 v164, 0
	v_mov_b32_e32 v165, 0
	v_mov_b32_e32 v166, 0
	v_mov_b32_e32 v167, 0
	v_mov_b32_e32 v168, 0
	v_mov_b32_e32 v169, 0
	v_mov_b32_e32 v170, 0
	v_mov_b32_e32 v171, 0
	v_mov_b32_e32 v172, 0
	v_mov_b32_e32 v173, 0
	v_mov_b32_e32 v174, 0
	v_mov_b32_e32 v175, 0
	v_mov_b32_e32 v144, 0
	v_mov_b32_e32 v145, 0
	v_mov_b32_e32 v146, 0
	v_mov_b32_e32 v147, 0
	v_mov_b32_e32 v148, 0
	v_mov_b32_e32 v149, 0
	v_mov_b32_e32 v150, 0
	v_mov_b32_e32 v151, 0
	v_mov_b32_e32 v152, 0
	v_mov_b32_e32 v153, 0
	v_mov_b32_e32 v154, 0
	v_mov_b32_e32 v155, 0
	v_mov_b32_e32 v156, 0
	v_mov_b32_e32 v157, 0
	v_mov_b32_e32 v158, 0
	v_mov_b32_e32 v159, 0
	s_cbranch_vccnz .LBB0_205
	s_andn2_b64 vcc, exec, s[42:43]
	s_mov_b64 s[42:43], -1
	s_cbranch_vccnz .LBB0_218
	v_add_u32_e32 v146, 0x21780, v219
	v_add_u32_e32 v147, 0x21708, v219
	v_add_u32_e32 v148, 0x21788, v219
	ds_read2_b32 v[144:145], v220 offset1:1
	ds_read2_b32 v[160:161], v146 offset1:1
	ds_read2_b32 v[146:147], v147 offset1:1
	ds_read2_b32 v[162:163], v148 offset1:1
	v_add_u32_e32 v148, 0x21720, v219
	v_add_u32_e32 v150, 0x217a0, v219
	v_add_u32_e32 v151, 0x21728, v219
	v_add_u32_e32 v152, 0x217a8, v219
	ds_read2_b32 v[148:149], v148 offset1:1
	ds_read2_b32 v[164:165], v150 offset1:1
	ds_read2_b32 v[150:151], v151 offset1:1
	ds_read2_b32 v[166:167], v152 offset1:1
	v_add_u32_e32 v152, 0x21740, v219
	v_add_u32_e32 v154, 0x217c0, v219
	v_add_u32_e32 v155, 0x21748, v219
	v_add_u32_e32 v156, 0x217c8, v219
	ds_read2_b32 v[152:153], v152 offset1:1
	ds_read2_b32 v[168:169], v154 offset1:1
	ds_read2_b32 v[154:155], v155 offset1:1
	ds_read2_b32 v[170:171], v156 offset1:1
	v_add_u32_e32 v156, 0x21760, v219
	v_add_u32_e32 v158, 0x217e0, v219
	v_add_u32_e32 v159, 0x21768, v219
	v_add_u32_e32 v174, 0x217e8, v219
	ds_read2_b32 v[156:157], v156 offset1:1
	ds_read2_b32 v[172:173], v158 offset1:1
	ds_read2_b32 v[158:159], v159 offset1:1
	ds_read2_b32 v[174:175], v174 offset1:1
	s_mov_b64 s[42:43], 0
